# stack F1 + P.V segment: 16 in-place v_fmamk_f32 score scalings per half-trip -> 8 v_pk_fma_f32 (same fma, broadcast scale/addend via op_sel)
# baseline (speedup 1.0000x reference)
.LBB0_757:
	s_add_i32 s6, 0, 0x12000
	v_add_u32_e32 v199, s6, v170
	v_add_u32_e32 v204, s6, v171
	v_add_u32_e32 v205, s6, v172
	ds_read_b128 v[64:67], v180 offset:49152
	ds_read_b128 v[68:71], v180 offset:57344
	ds_read_b128 v[200:203], v181 offset:49152
	ds_read_b128 v[226:229], v181 offset:57344
	ds_read_b128 v[230:233], v182 offset:49152
	ds_read_b128 v[234:237], v182 offset:57344
	ds_read_b128 v[238:241], v183 offset:49152
	ds_read_b128 v[242:245], v183 offset:57344
	s_waitcnt lgkmcnt(7)
	v_mfma_f32_32x32x16_bf16 v[80:95], v[64:67], v[124:127], 0
	s_add_i32 s12, s64, -1
	s_sub_i32 s80, s11, 64
	s_cmp_lt_u32 s12, 3
	s_cselect_b32 s80, s10, s80
	s_mul_i32 s81, s80, 0xc00
	s_add_i32 s85, s82, 0x8000
	s_mov_b32 m0, s85
	s_add_i32 s85, s82, 0x10000
	buffer_load_dwordx4 v154, s[72:75], s81 offen lds
	v_exp_f32_e32 v216, v128
	v_add_f32_e32 v128, 0, v222
	v_add_f32_e32 v128, v224, v128
	v_add_f32_e32 v128, v220, v128
	v_add_f32_e32 v128, v223, v128
	v_add_f32_e32 v128, v219, v128
	v_add_f32_e32 v128, v221, v128
	s_waitcnt lgkmcnt(6)
	v_mfma_f32_32x32x16_bf16 v[64:79], v[68:71], v[124:127], 0
	s_mov_b32 m0, s85
	s_add_i32 s85, s82, 0xa000
	buffer_load_dwordx4 v155, s[72:75], s81 offen lds
	v_add_f32_e32 v128, v217, v128
	v_add_f32_e32 v128, v218, v128
	v_add_f32_e32 v128, v212, v128
	v_add_f32_e32 v128, v214, v128
	v_add_f32_e32 v128, v211, v128
	v_add_f32_e32 v128, v213, v128
	v_exp_f32_e32 v138, v138
	s_waitcnt lgkmcnt(5)
	v_mfma_f32_32x32x16_bf16 v[80:95], v[200:203], v[120:123], v[80:95]
	s_mov_b32 m0, s85
	s_add_i32 s81, s81, 0x18000
	buffer_load_dwordx4 v154, s[72:75], s81 offen lds
	v_add_f32_e32 v128, v208, v128
	v_exp_f32_e32 v139, v139
	v_add_f32_e32 v128, v210, v128
	v_exp_f32_e32 v164, v136
	v_add_f32_e32 v128, v207, v128
	v_exp_f32_e32 v137, v137
	v_add_f32_e32 v128, v209, v128
	s_waitcnt lgkmcnt(4)
	v_mfma_f32_32x32x16_bf16 v[64:79], v[226:229], v[120:123], v[64:79]
	s_lshl_b32 s81, s83, 11
	s_add_i32 s85, s82, 0x4000
	s_mov_b32 m0, s85
	s_add_i32 s85, s82, 0x6000
	buffer_load_dwordx4 v158, s[76:79], s81 offen lds
	ds_read_b128 v[200:203], v184 offset:49152
	ds_read_b128 v[226:229], v184 offset:57344
	v_exp_f32_e32 v165, v132
	v_add_f32_e32 v128, v138, v128
	v_add_f32_e32 v128, v139, v128
	v_exp_f32_e32 v206, v130
	v_add_f32_e32 v128, v164, v128
	v_exp_f32_e32 v215, v131
	s_waitcnt lgkmcnt(5)
	v_mfma_f32_32x32x16_bf16 v[80:95], v[230:233], v[116:119], v[80:95]
	s_mov_b32 m0, s85
	s_add_i32 s81, s81, 0x10000
	buffer_load_dwordx4 v158, s[76:79], s81 offen lds
	s_mov_b32 s84, s80
	v_add_f32_e32 v128, v137, v128
	v_add_f32_e32 v128, v165, v128
	v_exp_f32_e32 v225, v129
	v_exp_f32_e32 v162, v162
	v_exp_f32_e32 v163, v163
	v_exp_f32_e32 v160, v160
	v_exp_f32_e32 v161, v161
	s_waitcnt lgkmcnt(4)
	v_mfma_f32_32x32x16_bf16 v[64:79], v[234:237], v[116:119], v[64:79]
	ds_read_b128 v[230:233], v185 offset:49152
	ds_read_b128 v[234:237], v185 offset:57344
	v_cvt_pk_bf16_f32 v129, v220, v223
	v_cvt_pk_bf16_f32 v130, v219, v221
	v_cvt_pk_bf16_f32 v131, v217, v218
	v_cvt_pk_bf16_f32 v132, v212, v214
	v_cvt_pk_bf16_f32 v136, v138, v139
	v_cvt_pk_bf16_f32 v137, v164, v137
	s_waitcnt lgkmcnt(5)
	v_mfma_f32_32x32x16_bf16 v[80:95], v[238:241], v[112:115], v[80:95]
	v_cvt_pk_bf16_f32 v139, v206, v215
	v_permlane32_swap_b32_e32 v129, v131
	s_nop 0
	v_permlane32_swap_b32_e32 v137, v139
	s_waitcnt lgkmcnt(4)
	v_mfma_f32_32x32x16_bf16 v[64:79], v[242:245], v[112:115], v[64:79]
	ds_read_b128 v[238:241], v186 offset:49152
	ds_read_b128 v[242:245], v186 offset:57344
	s_waitcnt lgkmcnt(5)
	v_mfma_f32_32x32x16_bf16 v[80:95], v[200:203], v[108:111], v[80:95]
	s_waitcnt lgkmcnt(4)
	v_mfma_f32_32x32x16_bf16 v[64:79], v[226:229], v[108:111], v[64:79]
	ds_read_b128 v[200:203], v187 offset:49152
	ds_read_b128 v[226:229], v187 offset:57344
	s_waitcnt lgkmcnt(5)
	v_mfma_f32_32x32x16_bf16 v[80:95], v[230:233], v[104:107], v[80:95]
	s_waitcnt lgkmcnt(4)
	v_mfma_f32_32x32x16_bf16 v[64:79], v[234:237], v[104:107], v[64:79]
	ds_read_b128 v[230:233], v199
	ds_read_b128 v[234:237], v199 offset:4096
	ds_read_b128 v[246:249], v190
	s_waitcnt lgkmcnt(6)
	v_mfma_f32_32x32x16_bf16 v[80:95], v[238:241], v[100:103], v[80:95]
	s_waitcnt lgkmcnt(5)
	v_mfma_f32_32x32x16_bf16 v[64:79], v[242:245], v[100:103], v[64:79]
	ds_read_b128 v[238:241], v204
	ds_read_b128 v[242:245], v204 offset:4096
	ds_read_b128 v[250:253], v190 offset:1024
	v_add_u32_e32 v204, s6, v173
	s_waitcnt lgkmcnt(7)
	v_mfma_f32_32x32x16_bf16 v[80:95], v[200:203], v[96:99], v[80:95]
	s_waitcnt lgkmcnt(6)
	v_mfma_f32_32x32x16_bf16 v[64:79], v[226:229], v[96:99], v[64:79]
	ds_read_b128 v[200:203], v205
	ds_read_b128 v[226:229], v205 offset:4096
	s_waitcnt lgkmcnt(5)
	v_mfma_f32_32x32x16_bf16 v[80:95], v[230:233], v[246:249], v[80:95]
	s_waitcnt lgkmcnt(5)
	v_mfma_f32_32x32x16_bf16 v[64:79], v[234:237], v[246:249], v[64:79]
	ds_read_b128 v[230:233], v204
	ds_read_b128 v[234:237], v204 offset:4096
	ds_read_b128 v[246:249], v190 offset:2048
	s_waitcnt lgkmcnt(5)
	v_mfma_f32_32x32x16_bf16 v[80:95], v[238:241], v[250:253], v[80:95]
	s_waitcnt lgkmcnt(5)
	v_mfma_f32_32x32x16_bf16 v[64:79], v[242:245], v[250:253], v[64:79]
	ds_read_b128 v[250:253], v190 offset:3072
	s_waitcnt lgkmcnt(1)
	v_mfma_f32_32x32x16_bf16 v[80:95], v[200:203], v[246:249], v[80:95]
	v_exp_f32_e32 v205, v133
	v_cvt_pk_bf16_f32 v133, v211, v213
	v_cvt_pk_bf16_f32 v138, v165, v205
	v_add_f32_e32 v128, v205, v128
	v_add_f32_e32 v128, v206, v128
	v_add_f32_e32 v128, v215, v128
	s_waitcnt lgkmcnt(1)
	v_mfma_f32_32x32x16_bf16 v[64:79], v[226:229], v[246:249], v[64:79]
	v_add_f32_e32 v128, v216, v128
	v_add_f32_e32 v128, v225, v128
	v_add_f32_e32 v128, v162, v128
	v_add_f32_e32 v128, v163, v128
	v_add_f32_e32 v128, v160, v128
	v_add_f32_e32 v128, v161, v128
	s_waitcnt lgkmcnt(0)
	v_mfma_f32_32x32x16_bf16 v[80:95], v[230:233], v[250:253], v[80:95]
	v_exp_f32_e32 v226, v134
	v_exp_f32_e32 v227, v135
	v_cvt_pk_bf16_f32 v134, v208, v210
	v_cvt_pk_bf16_f32 v135, v207, v209
	v_add_f32_e32 v128, v226, v128
	v_add_f32_e32 v203, v227, v128
	v_mov_b32_e32 v204, v203
	s_waitcnt lgkmcnt(0)
	v_mfma_f32_32x32x16_bf16 v[64:79], v[234:237], v[250:253], v[64:79]
	s_nop 0
	v_permlane32_swap_b32_e32 v203, v204
	v_cvt_pk_bf16_f32 v128, v222, v224
	v_cvt_pk_bf16_f32 v208, v216, v225
	v_cvt_pk_bf16_f32 v209, v162, v163
	v_cvt_pk_bf16_f32 v210, v160, v161
	v_cvt_pk_bf16_f32 v211, v226, v227
	v_permlane32_swap_b32_e32 v132, v134
	v_permlane32_swap_b32_e32 v128, v130
	v_permlane32_swap_b32_e32 v133, v135
	v_permlane32_swap_b32_e32 v136, v138
	v_permlane32_swap_b32_e32 v208, v210
	v_permlane32_swap_b32_e32 v209, v211
	ds_read_b64_tr_b16 v[160:161], v167 offset:0
	ds_read_b64_tr_b16 v[162:163], v167 offset:0x800
	ds_read_b64_tr_b16 v[232:233], v167 offset:0x1000
	ds_read_b64_tr_b16 v[234:235], v167 offset:0x1800
	ds_read_b64_tr_b16 v[236:237], v167 offset:0x2000
	ds_read_b64_tr_b16 v[238:239], v167 offset:0x2800
	ds_read_b64_tr_b16 v[240:241], v167 offset:0x3000
	ds_read_b64_tr_b16 v[242:243], v167 offset:0x3800
	v_max_f32_e32 v164, v81, v81
	v_max_f32_e32 v165, v80, v80
	v_max_f32_e32 v164, v165, v164
	v_max3_f32 v164, v164, v82, v83
	v_max3_f32 v164, v164, v84, v85
	v_max3_f32 v164, v164, v86, v87
	v_max3_f32 v164, v164, v88, v89
	v_max3_f32 v164, v164, v90, v91
	v_max3_f32 v164, v164, v92, v93
	v_max3_f32 v164, v164, v94, v95
	s_waitcnt lgkmcnt(0)
	v_mfma_f32_32x32x16_bf16 v[16:31], v[128:131], v[160:163], v[16:31]
	v_max3_f32 v160, v164, v64, v65
	v_max3_f32 v160, v160, v66, v67
	v_max3_f32 v160, v160, v68, v69
	v_mfma_f32_32x32x16_bf16 v[16:31], v[132:135], v[232:235], v[16:31]
	ds_read_b64_tr_b16 v[232:233], v167 offset:0x200
	ds_read_b64_tr_b16 v[234:235], v167 offset:0xa00
	v_max3_f32 v160, v160, v70, v71
	v_max3_f32 v160, v160, v72, v73
	v_max3_f32 v160, v160, v74, v75
	v_mfma_f32_32x32x16_bf16 v[16:31], v[136:139], v[236:239], v[16:31]
	ds_read_b64_tr_b16 v[236:237], v167 offset:0x1200
	ds_read_b64_tr_b16 v[238:239], v167 offset:0x1a00
	ds_read_b64_tr_b16 v[244:245], v167 offset:0x2200
	ds_read_b64_tr_b16 v[246:247], v167 offset:0x2a00
	ds_read_b64_tr_b16 v[248:249], v167 offset:0x3200
	ds_read_b64_tr_b16 v[250:251], v167 offset:0x3a00
	v_max3_f32 v160, v160, v76, v77
	v_max3_f32 v160, v160, v78, v79
	v_mov_b32_e32 v161, v160
	v_mfma_f32_32x32x16_bf16 v[16:31], v[208:211], v[240:243], v[16:31]
	v_max_f32_e32 v162, v198, v198
	v_permlane32_swap_b32_e32 v160, v161
	v_max_f32_e32 v161, v161, v161
	v_max_f32_e32 v160, v160, v160
	v_max_f32_e32 v160, v160, v161
	s_waitcnt lgkmcnt(0)
	v_mfma_f32_32x32x16_bf16 v[32:47], v[128:131], v[232:235], v[32:47]
	ds_read_b64_tr_b16 v[232:233], v167 offset:0x400
	ds_read_b64_tr_b16 v[234:235], v167 offset:0xc00
	v_sub_f32_e32 v161, v160, v198
	v_max_f32_e32 v160, v162, v160
	v_sub_f32_e32 v162, v198, v160
	v_mul_f32_e32 v162, 0x3dd53b94, v162
	v_exp_f32_e32 v162, v162
	v_mfma_f32_32x32x16_bf16 v[32:47], v[132:135], v[236:239], v[32:47]
	ds_read_b64_tr_b16 v[236:237], v167 offset:0x1400
	ds_read_b64_tr_b16 v[238:239], v167 offset:0x1c00
	ds_read_b64_tr_b16 v[240:241], v167 offset:0x2400
	ds_read_b64_tr_b16 v[242:243], v167 offset:0x2c00
	v_cmp_ge_f32_e32 vcc, s48, v161
	s_cmp_eq_u64 vcc, exec
	s_cselect_b64 s[6:7], -1, 0
	v_cndmask_b32_e64 v206, v162, 1.0, s[6:7]
	v_cndmask_b32_e64 v160, v160, v198, s[6:7]
	v_mul_f32_e32 v205, 0xbdd53b94, v160
	v_cmp_gt_f32_e32 vcc, 1.0, v206
	v_mfma_f32_32x32x16_bf16 v[32:47], v[136:139], v[244:247], v[32:47]
	ds_read_b64_tr_b16 v[244:245], v167 offset:0x3400
	ds_read_b64_tr_b16 v[246:247], v167 offset:0x3c00
	v_pk_fma_f32 v[86:87], v[86:87], s[28:29], v[204:205] op_sel:[0,0,1] op_sel_hi:[1,0,1]
	v_pk_fma_f32 v[80:81], v[80:81], s[28:29], v[204:205] op_sel:[0,0,1] op_sel_hi:[1,0,1]
	v_pk_fma_f32 v[82:83], v[82:83], s[28:29], v[204:205] op_sel:[0,0,1] op_sel_hi:[1,0,1]
	v_mfma_f32_32x32x16_bf16 v[32:47], v[208:211], v[248:251], v[32:47]
	v_pk_fma_f32 v[84:85], v[84:85], s[28:29], v[204:205] op_sel:[0,0,1] op_sel_hi:[1,0,1]
	v_pk_fma_f32 v[88:89], v[88:89], s[28:29], v[204:205] op_sel:[0,0,1] op_sel_hi:[1,0,1]
	s_waitcnt lgkmcnt(0)
	v_mfma_f32_32x32x16_bf16 v[0:15], v[128:131], v[232:235], v[0:15]
	ds_read_b64_tr_b16 v[232:233], v167 offset:0x600
	ds_read_b64_tr_b16 v[234:235], v167 offset:0xe00
	v_pk_fma_f32 v[90:91], v[90:91], s[28:29], v[204:205] op_sel:[0,0,1] op_sel_hi:[1,0,1]
	v_pk_fma_f32 v[92:93], v[92:93], s[28:29], v[204:205] op_sel:[0,0,1] op_sel_hi:[1,0,1]
	v_pk_fma_f32 v[94:95], v[94:95], s[28:29], v[204:205] op_sel:[0,0,1] op_sel_hi:[1,0,1]
	v_mfma_f32_32x32x16_bf16 v[0:15], v[132:135], v[236:239], v[0:15]
	ds_read_b64_tr_b16 v[236:237], v167 offset:0x1600
	ds_read_b64_tr_b16 v[238:239], v167 offset:0x1e00
	v_fmamk_f32 v215, v64, 0x3dd53b94, v205
	v_fmamk_f32 v216, v65, 0x3dd53b94, v205
	v_fmamk_f32 v217, v66, 0x3dd53b94, v205
	v_fmamk_f32 v218, v67, 0x3dd53b94, v205
	v_mfma_f32_32x32x16_bf16 v[0:15], v[136:139], v[240:243], v[0:15]
	ds_read_b64_tr_b16 v[240:241], v167 offset:0x2600
	ds_read_b64_tr_b16 v[242:243], v167 offset:0x2e00
	ds_read_b64_tr_b16 v[248:249], v167 offset:0x3600
	ds_read_b64_tr_b16 v[250:251], v167 offset:0x3e00
	v_fmamk_f32 v219, v68, 0x3dd53b94, v205
	v_fmamk_f32 v212, v73, 0x3dd53b94, v205
	v_fmamk_f32 v213, v74, 0x3dd53b94, v205
	v_fmamk_f32 v214, v75, 0x3dd53b94, v205
	v_mfma_f32_32x32x16_bf16 v[0:15], v[208:211], v[244:247], v[0:15]
	v_fmamk_f32 v207, v76, 0x3dd53b94, v205
	v_fmamk_f32 v220, v77, 0x3dd53b94, v205
	v_fmamk_f32 v221, v78, 0x3dd53b94, v205
	s_waitcnt lgkmcnt(0)
	v_mfma_f32_32x32x16_bf16 v[48:63], v[128:131], v[232:235], v[48:63]
	v_exp_f32_e32 v128, v80
	v_exp_f32_e32 v129, v82
	v_exp_f32_e32 v130, v84
	v_exp_f32_e32 v131, v86
	v_mfma_f32_32x32x16_bf16 v[48:63], v[132:135], v[236:239], v[48:63]
	v_exp_f32_e32 v132, v88
	v_exp_f32_e32 v133, v90
	v_exp_f32_e32 v134, v92
	v_exp_f32_e32 v135, v94
	v_mfma_f32_32x32x16_bf16 v[48:63], v[136:139], v[240:243], v[48:63]
	v_exp_f32_e32 v139, v89
	v_exp_f32_e32 v138, v91
	v_exp_f32_e32 v137, v93
	v_exp_f32_e32 v136, v95
	v_mfma_f32_32x32x16_bf16 v[48:63], v[208:211], v[248:251], v[48:63]
	v_exp_f32_e32 v161, v87
	v_exp_f32_e32 v198, v81
	v_exp_f32_e32 v163, v83
	v_exp_f32_e32 v162, v85
	v_fmamk_f32 v208, v69, 0x3dd53b94, v205
	v_fmamk_f32 v209, v70, 0x3dd53b94, v205
	v_fmamk_f32 v210, v71, 0x3dd53b94, v205
	v_fmamk_f32 v211, v72, 0x3dd53b94, v205
	v_fmac_f32_e32 v205, 0x3dd53b94, v79
	s_cbranch_vccz .LBB0_761
	s_and_saveexec_b64 s[8:9], s[4:5]
	ds_write_b32 v189, v206 offset:128
	s_or_b64 exec, exec, s[8:9]
	s_waitcnt lgkmcnt(0)
	v_add_u32_e32 v248, s62, v169
	ds_read_b128 v[232:235], v248 offset:224
	ds_read_b128 v[236:239], v248 offset:192
	ds_read_b128 v[240:243], v248 offset:160
	ds_read_b128 v[244:247], v248 offset:128
	s_waitcnt lgkmcnt(3)
	v_pk_mul_f32 v[28:29], v[28:29], v[232:233]
	s_waitcnt lgkmcnt(2)
	v_pk_mul_f32 v[24:25], v[24:25], v[236:237]
	s_waitcnt lgkmcnt(1)
	v_pk_mul_f32 v[20:21], v[20:21], v[240:241]
	v_pk_mul_f32 v[30:31], v[30:31], v[234:235]
	v_pk_mul_f32 v[26:27], v[26:27], v[238:239]
	v_pk_mul_f32 v[22:23], v[22:23], v[242:243]
	s_waitcnt lgkmcnt(0)
	v_pk_mul_f32 v[18:19], v[18:19], v[246:247]
	v_pk_mul_f32 v[16:17], v[16:17], v[244:245]
	v_pk_mul_f32 v[44:45], v[44:45], v[232:233]
	v_pk_mul_f32 v[40:41], v[40:41], v[236:237]
	v_pk_mul_f32 v[36:37], v[36:37], v[240:241]
	v_pk_mul_f32 v[46:47], v[46:47], v[234:235]
	v_pk_mul_f32 v[42:43], v[42:43], v[238:239]
	v_pk_mul_f32 v[38:39], v[38:39], v[242:243]
	v_pk_mul_f32 v[34:35], v[34:35], v[246:247]
	v_pk_mul_f32 v[32:33], v[32:33], v[244:245]
	v_pk_mul_f32 v[12:13], v[12:13], v[232:233]
	v_pk_mul_f32 v[8:9], v[8:9], v[236:237]
	v_pk_mul_f32 v[4:5], v[4:5], v[240:241]
	v_pk_mul_f32 v[14:15], v[14:15], v[234:235]
	v_pk_mul_f32 v[10:11], v[10:11], v[238:239]
	v_pk_mul_f32 v[6:7], v[6:7], v[242:243]
	v_pk_mul_f32 v[2:3], v[2:3], v[246:247]
	v_pk_mul_f32 v[0:1], v[0:1], v[244:245]
	v_pk_mul_f32 v[60:61], v[60:61], v[232:233]
	v_pk_mul_f32 v[56:57], v[56:57], v[236:237]
	v_pk_mul_f32 v[52:53], v[52:53], v[240:241]
	v_pk_mul_f32 v[62:63], v[62:63], v[234:235]
	v_pk_mul_f32 v[58:59], v[58:59], v[238:239]
	v_pk_mul_f32 v[54:55], v[54:55], v[242:243]
	v_pk_mul_f32 v[50:51], v[50:51], v[246:247]
	v_pk_mul_f32 v[48:49], v[48:49], v[244:245]
.LBB0_761:
	s_waitcnt vmcnt(0) lgkmcnt(0)
	s_barrier
	ds_read_b128 v[64:67], v180 offset:32768
	ds_read_b128 v[68:71], v180 offset:40960
	ds_read_b128 v[222:225], v181 offset:32768
	ds_read_b128 v[226:229], v181 offset:40960
	ds_read_b128 v[230:233], v182 offset:32768
	ds_read_b128 v[234:237], v182 offset:40960
	ds_read_b128 v[238:241], v183 offset:32768
	ds_read_b128 v[242:245], v183 offset:40960
	v_exp_f32_e32 v164, v215
	v_add_f32_e32 v215, 0, v128
	s_waitcnt lgkmcnt(7)
	v_mfma_f32_32x32x16_bf16 v[80:95], v[64:67], v[124:127], 0
	s_add_i32 s80, s10, 64
	s_cmp_lt_u32 s12, 2
	s_cselect_b32 s80, s80, s11
	s_mul_i32 s81, s80, 0xc00
	s_add_i32 s85, s82, 0xc000
	s_mov_b32 m0, s85
	s_add_i32 s85, s82, 0x12000
	buffer_load_dwordx4 v154, s[72:75], s81 offen lds
	v_add_f32_e32 v215, v198, v215
	v_add_f32_e32 v215, v129, v215
	v_add_f32_e32 v215, v163, v215
	v_add_f32_e32 v215, v130, v215
	v_add_f32_e32 v215, v162, v215
	v_add_f32_e32 v215, v131, v215
	v_add_f32_e32 v215, v161, v215
	s_waitcnt lgkmcnt(6)
	v_mfma_f32_32x32x16_bf16 v[64:79], v[68:71], v[124:127], 0
	s_mov_b32 m0, s85
	s_add_i32 s85, s82, 0xe000
	buffer_load_dwordx4 v155, s[72:75], s81 offen lds
	v_add_f32_e32 v215, v132, v215
	v_add_f32_e32 v215, v139, v215
	v_add_f32_e32 v215, v133, v215
	v_add_f32_e32 v215, v138, v215
	v_add_f32_e32 v215, v134, v215
	v_exp_f32_e32 v165, v216
	v_add_f32_e32 v215, v137, v215
	s_waitcnt lgkmcnt(5)
	v_mfma_f32_32x32x16_bf16 v[80:95], v[222:225], v[120:123], v[80:95]
	s_mov_b32 m0, s85
	s_add_i32 s81, s81, 0x18000
	buffer_load_dwordx4 v154, s[72:75], s81 offen lds
	v_exp_f32_e32 v217, v217
	v_add_f32_e32 v215, v135, v215
	v_exp_f32_e32 v218, v218
	v_add_f32_e32 v215, v136, v215
	v_exp_f32_e32 v219, v219
	v_add_f32_e32 v215, v164, v215
	v_exp_f32_e32 v208, v208
	s_waitcnt lgkmcnt(4)
	v_mfma_f32_32x32x16_bf16 v[64:79], v[226:229], v[120:123], v[64:79]
	s_lshl_b32 s81, s84, 11
	s_add_i32 s85, s82, 0x0
	s_mov_b32 m0, s85
	s_add_i32 s85, s82, 0x2000
	buffer_load_dwordx4 v158, s[76:79], s81 offen lds
	ds_read_b128 v[222:225], v184 offset:32768
	ds_read_b128 v[226:229], v184 offset:40960
	v_add_f32_e32 v215, v165, v215
	v_exp_f32_e32 v209, v209
	v_add_f32_e32 v215, v217, v215
	v_exp_f32_e32 v210, v210
	v_add_f32_e32 v215, v218, v215
	v_exp_f32_e32 v211, v211
	s_waitcnt lgkmcnt(5)
	v_mfma_f32_32x32x16_bf16 v[80:95], v[230:233], v[116:119], v[80:95]
	s_mov_b32 m0, s85
	s_add_i32 s81, s81, 0x10000
	buffer_load_dwordx4 v158, s[76:79], s81 offen lds
	s_mov_b32 s83, s80
	v_add_f32_e32 v215, v219, v215
	v_exp_f32_e32 v212, v212
	v_add_f32_e32 v215, v208, v215
	v_exp_f32_e32 v213, v213
	v_add_f32_e32 v215, v209, v215
	v_exp_f32_e32 v214, v214
	v_add_f32_e32 v215, v210, v215
	s_waitcnt lgkmcnt(4)
	v_mfma_f32_32x32x16_bf16 v[64:79], v[234:237], v[116:119], v[64:79]
	ds_read_b128 v[230:233], v185 offset:32768
	ds_read_b128 v[234:237], v185 offset:40960
	v_exp_f32_e32 v207, v207
	v_add_f32_e32 v215, v211, v215
	v_exp_f32_e32 v220, v220
	v_add_f32_e32 v215, v212, v215
	v_exp_f32_e32 v221, v221
	v_add_f32_e32 v215, v213, v215
	s_waitcnt lgkmcnt(5)
	v_mfma_f32_32x32x16_bf16 v[80:95], v[238:241], v[112:115], v[80:95]
	v_exp_f32_e32 v205, v205
	v_add_f32_e32 v215, v214, v215
	v_add_f32_e32 v215, v207, v215
	v_add_f32_e32 v215, v220, v215
	v_add_f32_e32 v215, v221, v215
	v_add_f32_e32 v215, v205, v215
	v_mov_b32_e32 v216, v215
	s_waitcnt lgkmcnt(4)
	v_mfma_f32_32x32x16_bf16 v[64:79], v[242:245], v[112:115], v[64:79]
	ds_read_b128 v[238:241], v186 offset:32768
	ds_read_b128 v[242:245], v186 offset:40960
	v_permlane32_swap_b32_e32 v215, v216
	v_cvt_pk_bf16_f32 v128, v128, v198
	v_cvt_pk_bf16_f32 v129, v129, v163
	v_cvt_pk_bf16_f32 v130, v130, v162
	v_cvt_pk_bf16_f32 v131, v131, v161
	s_waitcnt lgkmcnt(5)
	v_mfma_f32_32x32x16_bf16 v[80:95], v[222:225], v[108:111], v[80:95]
	v_cvt_pk_bf16_f32 v132, v132, v139
	v_cvt_pk_bf16_f32 v133, v133, v138
	v_cvt_pk_bf16_f32 v134, v134, v137
	v_cvt_pk_bf16_f32 v135, v135, v136
	v_cvt_pk_bf16_f32 v136, v164, v165
	v_cvt_pk_bf16_f32 v137, v217, v218
	v_cvt_pk_bf16_f32 v138, v219, v208
	s_waitcnt lgkmcnt(4)
	v_mfma_f32_32x32x16_bf16 v[64:79], v[226:229], v[108:111], v[64:79]
	ds_read_b128 v[222:225], v187 offset:32768
	ds_read_b128 v[226:229], v187 offset:40960
	v_cvt_pk_bf16_f32 v139, v209, v210
	v_cvt_pk_bf16_f32 v208, v211, v212
	v_cvt_pk_bf16_f32 v209, v213, v214
	v_cvt_pk_bf16_f32 v210, v207, v220
	v_cvt_pk_bf16_f32 v211, v221, v205
	v_permlane32_swap_b32_e32 v128, v130
	s_waitcnt lgkmcnt(5)
	v_mfma_f32_32x32x16_bf16 v[80:95], v[230:233], v[104:107], v[80:95]
	v_permlane32_swap_b32_e32 v129, v131
	v_permlane32_swap_b32_e32 v132, v134
	v_permlane32_swap_b32_e32 v133, v135
	v_permlane32_swap_b32_e32 v136, v138
	s_waitcnt lgkmcnt(4)
	v_mfma_f32_32x32x16_bf16 v[64:79], v[234:237], v[104:107], v[64:79]
	ds_read_b128 v[230:233], v191
	ds_read_b128 v[234:237], v191 offset:4096
	ds_read_b128 v[246:249], v190
	v_permlane32_swap_b32_e32 v137, v139
	v_permlane32_swap_b32_e32 v208, v210
	v_permlane32_swap_b32_e32 v209, v211
	s_waitcnt lgkmcnt(6)
	v_mfma_f32_32x32x16_bf16 v[80:95], v[238:241], v[100:103], v[80:95]
	s_waitcnt lgkmcnt(5)
	v_mfma_f32_32x32x16_bf16 v[64:79], v[242:245], v[100:103], v[64:79]
	ds_read_b128 v[238:241], v192
	ds_read_b128 v[242:245], v192 offset:4096
	ds_read_b128 v[250:253], v190 offset:1024
	s_waitcnt lgkmcnt(7)
	v_mfma_f32_32x32x16_bf16 v[80:95], v[222:225], v[96:99], v[80:95]
	s_waitcnt lgkmcnt(6)
	v_mfma_f32_32x32x16_bf16 v[64:79], v[226:229], v[96:99], v[64:79]
	ds_read_b128 v[222:225], v193
	ds_read_b128 v[226:229], v193 offset:4096
	s_waitcnt lgkmcnt(5)
	v_mfma_f32_32x32x16_bf16 v[80:95], v[230:233], v[246:249], v[80:95]
	s_waitcnt lgkmcnt(5)
	v_mfma_f32_32x32x16_bf16 v[64:79], v[234:237], v[246:249], v[64:79]
	ds_read_b128 v[230:233], v194
	ds_read_b128 v[234:237], v194 offset:4096
	ds_read_b128 v[246:249], v190 offset:2048
	s_waitcnt lgkmcnt(5)
	v_mfma_f32_32x32x16_bf16 v[80:95], v[238:241], v[250:253], v[80:95]
	s_waitcnt lgkmcnt(5)
	v_mfma_f32_32x32x16_bf16 v[64:79], v[242:245], v[250:253], v[64:79]
	ds_read_b128 v[250:253], v190 offset:3072
	s_waitcnt lgkmcnt(1)
	v_mfma_f32_32x32x16_bf16 v[80:95], v[222:225], v[246:249], v[80:95]
	s_waitcnt lgkmcnt(1)
	v_mfma_f32_32x32x16_bf16 v[64:79], v[226:229], v[246:249], v[64:79]
	s_waitcnt lgkmcnt(0)
	v_mfma_f32_32x32x16_bf16 v[80:95], v[230:233], v[250:253], v[80:95]
	s_waitcnt lgkmcnt(0)
	v_mfma_f32_32x32x16_bf16 v[64:79], v[234:237], v[250:253], v[64:79]
	ds_read_b64_tr_b16 v[238:239], v174 offset:0
	ds_read_b64_tr_b16 v[240:241], v174 offset:0x800
	ds_read_b64_tr_b16 v[242:243], v174 offset:0x1000
	ds_read_b64_tr_b16 v[244:245], v174 offset:0x1800
	ds_read_b64_tr_b16 v[246:247], v174 offset:0x2000
	ds_read_b64_tr_b16 v[248:249], v174 offset:0x2800
	ds_read_b64_tr_b16 v[250:251], v174 offset:0x3000
	ds_read_b64_tr_b16 v[252:253], v174 offset:0x3800
	s_nop 3
	v_max_f32_e32 v161, v81, v81
	v_max_f32_e32 v162, v80, v80
	v_max_f32_e32 v161, v162, v161
	v_max3_f32 v161, v161, v82, v83
	v_max3_f32 v161, v161, v84, v85
	v_max3_f32 v161, v161, v86, v87
	v_max3_f32 v161, v161, v88, v89
	v_max3_f32 v161, v161, v90, v91
	v_max3_f32 v161, v161, v92, v93
	v_max3_f32 v161, v161, v94, v95
	s_waitcnt lgkmcnt(0)
	v_mfma_f32_32x32x16_bf16 v[16:31], v[128:131], v[238:241], v[16:31]
	ds_read_b64_tr_b16 v[238:239], v174 offset:0x200
	ds_read_b64_tr_b16 v[240:241], v174 offset:0xa00
	v_max3_f32 v161, v161, v64, v65
	v_max3_f32 v161, v161, v66, v67
	v_max3_f32 v161, v161, v68, v69
	v_mfma_f32_32x32x16_bf16 v[16:31], v[132:135], v[242:245], v[16:31]
	ds_read_b64_tr_b16 v[242:243], v174 offset:0x1200
	ds_read_b64_tr_b16 v[244:245], v174 offset:0x1a00
	v_max3_f32 v161, v161, v70, v71
	v_max3_f32 v161, v161, v72, v73
	v_max3_f32 v161, v161, v74, v75
	v_mfma_f32_32x32x16_bf16 v[16:31], v[136:139], v[246:249], v[16:31]
	ds_read_b64_tr_b16 v[246:247], v174 offset:0x2200
	ds_read_b64_tr_b16 v[248:249], v174 offset:0x2a00
	ds_read_b64_tr_b16 v[162:163], v174 offset:0x3200
	ds_read_b64_tr_b16 v[164:165], v174 offset:0x3a00
	v_max3_f32 v161, v161, v76, v77
	v_max3_f32 v161, v161, v78, v79
	v_mov_b32_e32 v198, v161
	v_mfma_f32_32x32x16_bf16 v[16:31], v[208:211], v[250:253], v[16:31]
	v_max_f32_e32 v205, v160, v160
	v_permlane32_swap_b32_e32 v161, v198
	v_max_f32_e32 v198, v198, v198
	v_max_f32_e32 v161, v161, v161
	v_max_f32_e32 v161, v161, v198
	s_waitcnt lgkmcnt(0)
	v_mfma_f32_32x32x16_bf16 v[32:47], v[128:131], v[238:241], v[32:47]
	ds_read_b64_tr_b16 v[238:239], v174 offset:0x400
	ds_read_b64_tr_b16 v[240:241], v174 offset:0xc00
	v_sub_f32_e32 v198, v161, v160
	v_max_f32_e32 v161, v205, v161
	v_sub_f32_e32 v205, v160, v161
	v_mul_f32_e32 v205, 0x3dd53b94, v205
	v_exp_f32_e32 v205, v205
	v_mfma_f32_32x32x16_bf16 v[32:47], v[132:135], v[242:245], v[32:47]
	ds_read_b64_tr_b16 v[242:243], v174 offset:0x1400
	ds_read_b64_tr_b16 v[244:245], v174 offset:0x1c00
	v_cmp_ge_f32_e32 vcc, s48, v198
	s_cmp_eq_u64 vcc, exec
	s_cselect_b64 s[6:7], -1, 0
	v_cndmask_b32_e64 v205, v205, 1.0, s[6:7]
	v_cndmask_b32_e64 v198, v161, v160, s[6:7]
	v_mul_f32_e32 v236, 0xbdd53b94, v198
	v_mov_b32_e32 v237, v236
	v_cmp_gt_f32_e32 vcc, 1.0, v205
	v_mfma_f32_32x32x16_bf16 v[32:47], v[136:139], v[246:249], v[32:47]
	ds_read_b64_tr_b16 v[246:247], v174 offset:0x2400
	ds_read_b64_tr_b16 v[248:249], v174 offset:0x2c00
	ds_read_b64_tr_b16 v[250:251], v174 offset:0x3400
	ds_read_b64_tr_b16 v[252:253], v174 offset:0x3c00
	v_pk_fma_f32 v[80:81], v[80:81], s[28:29], v[236:237] op_sel_hi:[1,0,0]
	v_pk_fma_f32 v[82:83], v[82:83], s[28:29], v[236:237] op_sel_hi:[1,0,0]
	v_mfma_f32_32x32x16_bf16 v[32:47], v[208:211], v[162:165], v[32:47]
	v_pk_fma_f32 v[84:85], v[84:85], s[28:29], v[236:237] op_sel_hi:[1,0,0]
	v_pk_fma_f32 v[86:87], v[86:87], s[28:29], v[236:237] op_sel_hi:[1,0,0]
	s_waitcnt lgkmcnt(0)
	v_mfma_f32_32x32x16_bf16 v[0:15], v[128:131], v[238:241], v[0:15]
	ds_read_b64_tr_b16 v[162:163], v174 offset:0x600
	ds_read_b64_tr_b16 v[164:165], v174 offset:0xe00
	ds_read_b64_tr_b16 v[238:239], v174 offset:0x1600
	ds_read_b64_tr_b16 v[240:241], v174 offset:0x1e00
	v_pk_fma_f32 v[88:89], v[88:89], s[28:29], v[236:237] op_sel_hi:[1,0,0]
	v_pk_fma_f32 v[90:91], v[90:91], s[28:29], v[236:237] op_sel_hi:[1,0,0]
	v_mfma_f32_32x32x16_bf16 v[0:15], v[132:135], v[242:245], v[0:15]
	ds_read_b64_tr_b16 v[242:243], v174 offset:0x2600
	ds_read_b64_tr_b16 v[244:245], v174 offset:0x2e00
	v_pk_fma_f32 v[92:93], v[92:93], s[28:29], v[236:237] op_sel_hi:[1,0,0]
	v_pk_fma_f32 v[94:95], v[94:95], s[28:29], v[236:237] op_sel_hi:[1,0,0]
	v_mfma_f32_32x32x16_bf16 v[0:15], v[136:139], v[246:249], v[0:15]
	ds_read_b64_tr_b16 v[246:247], v174 offset:0x3600
	ds_read_b64_tr_b16 v[248:249], v174 offset:0x3e00
	v_exp_f32_e32 v222, v80
	v_exp_f32_e32 v224, v81
	v_exp_f32_e32 v220, v82
	v_mfma_f32_32x32x16_bf16 v[0:15], v[208:211], v[250:253], v[0:15]
	v_exp_f32_e32 v223, v83
	v_exp_f32_e32 v219, v84
	v_exp_f32_e32 v221, v85
	s_waitcnt lgkmcnt(0)
	v_mfma_f32_32x32x16_bf16 v[48:63], v[128:131], v[162:165], v[48:63]
	v_exp_f32_e32 v217, v86
	v_exp_f32_e32 v218, v87
	v_exp_f32_e32 v212, v88
	v_pk_fma_f32 v[130:131], v[70:71], s[28:29], v[236:237] op_sel_hi:[1,0,0]
	v_pk_fma_f32 v[128:129], v[72:73], s[28:29], v[236:237] op_sel_hi:[1,0,0]
	v_mfma_f32_32x32x16_bf16 v[48:63], v[132:135], v[238:241], v[48:63]
	v_exp_f32_e32 v214, v89
	v_exp_f32_e32 v213, v91
	v_exp_f32_e32 v207, v94
	v_pk_fma_f32 v[132:133], v[68:69], s[28:29], v[236:237] op_sel_hi:[1,0,0]
	v_pk_fma_f32 v[134:135], v[78:79], s[28:29], v[236:237] op_sel_hi:[1,0,0]
	v_mfma_f32_32x32x16_bf16 v[48:63], v[136:139], v[242:245], v[48:63]
	v_pk_fma_f32 v[138:139], v[64:65], s[28:29], v[236:237] op_sel_hi:[1,0,0]
	v_pk_fma_f32 v[136:137], v[66:67], s[28:29], v[236:237] op_sel_hi:[1,0,0]
	v_pk_fma_f32 v[162:163], v[74:75], s[28:29], v[236:237] op_sel_hi:[1,0,0]
	v_pk_fma_f32 v[160:161], v[76:77], s[28:29], v[236:237] op_sel_hi:[1,0,0]
	v_mfma_f32_32x32x16_bf16 v[48:63], v[208:211], v[246:249], v[48:63]
	v_exp_f32_e32 v211, v90
	v_exp_f32_e32 v208, v92
	v_exp_f32_e32 v210, v93
	v_exp_f32_e32 v209, v95
	v_add_f32_e32 v64, v203, v204
	v_fmac_f32_e32 v64, v197, v140
	v_add_f32_e32 v140, v215, v216
	s_addk_i32 s10, 0x80
	s_add_i32 s64, s64, 2
	s_addk_i32 s11, 0x80
	v_fmac_f32_e32 v140, v64, v206
	s_cbranch_vccz .LBB0_765
	s_and_saveexec_b64 s[8:9], s[4:5]
	ds_write_b32 v189, v205 offset:128
	s_or_b64 exec, exec, s[8:9]
	s_waitcnt lgkmcnt(0)
	v_add_u32_e32 v164, s62, v169
	ds_read_b128 v[238:241], v164 offset:224
	ds_read_b128 v[242:245], v164 offset:192
	ds_read_b128 v[246:249], v164 offset:160
	ds_read_b128 v[250:253], v164 offset:128
	s_waitcnt lgkmcnt(3)
	v_pk_mul_f32 v[28:29], v[28:29], v[238:239]
	s_waitcnt lgkmcnt(2)
	v_pk_mul_f32 v[24:25], v[24:25], v[242:243]
	s_waitcnt lgkmcnt(1)
	v_pk_mul_f32 v[20:21], v[20:21], v[246:247]
	v_pk_mul_f32 v[30:31], v[30:31], v[240:241]
	v_pk_mul_f32 v[26:27], v[26:27], v[244:245]
	v_pk_mul_f32 v[22:23], v[22:23], v[248:249]
	s_waitcnt lgkmcnt(0)
	v_pk_mul_f32 v[18:19], v[18:19], v[252:253]
	v_pk_mul_f32 v[16:17], v[16:17], v[250:251]
	v_pk_mul_f32 v[44:45], v[44:45], v[238:239]
	v_pk_mul_f32 v[40:41], v[40:41], v[242:243]
	v_pk_mul_f32 v[36:37], v[36:37], v[246:247]
	v_pk_mul_f32 v[46:47], v[46:47], v[240:241]
	v_pk_mul_f32 v[42:43], v[42:43], v[244:245]
	v_pk_mul_f32 v[38:39], v[38:39], v[248:249]
	v_pk_mul_f32 v[34:35], v[34:35], v[252:253]
	v_pk_mul_f32 v[32:33], v[32:33], v[250:251]
	v_pk_mul_f32 v[12:13], v[12:13], v[238:239]
	v_pk_mul_f32 v[8:9], v[8:9], v[242:243]
	v_pk_mul_f32 v[4:5], v[4:5], v[246:247]
	v_pk_mul_f32 v[14:15], v[14:15], v[240:241]
	v_pk_mul_f32 v[10:11], v[10:11], v[244:245]
	v_pk_mul_f32 v[6:7], v[6:7], v[248:249]
	v_pk_mul_f32 v[2:3], v[2:3], v[252:253]
	v_pk_mul_f32 v[0:1], v[0:1], v[250:251]
	v_pk_mul_f32 v[60:61], v[60:61], v[238:239]
	v_pk_mul_f32 v[56:57], v[56:57], v[242:243]
	v_pk_mul_f32 v[52:53], v[52:53], v[246:247]
	v_pk_mul_f32 v[62:63], v[62:63], v[240:241]
	v_pk_mul_f32 v[58:59], v[58:59], v[244:245]
	v_pk_mul_f32 v[54:55], v[54:55], v[248:249]
	v_pk_mul_f32 v[50:51], v[50:51], v[252:253]
	v_pk_mul_f32 v[48:49], v[48:49], v[250:251]

.LBB0_2012:
	s_add_i32 s6, 0, 0x12000
	v_add_u32_e32 v199, s6, v170
	v_add_u32_e32 v204, s6, v171
	v_add_u32_e32 v205, s6, v172
	ds_read_b128 v[64:67], v180 offset:49152
	ds_read_b128 v[68:71], v180 offset:57344
	ds_read_b128 v[200:203], v181 offset:49152
	ds_read_b128 v[226:229], v181 offset:57344
	ds_read_b128 v[230:233], v182 offset:49152
	ds_read_b128 v[234:237], v182 offset:57344
	ds_read_b128 v[238:241], v183 offset:49152
	ds_read_b128 v[242:245], v183 offset:57344
	s_waitcnt lgkmcnt(7)
	v_mfma_f32_32x32x16_bf16 v[80:95], v[64:67], v[124:127], 0
	s_add_i32 s8, s8, 2
	s_sub_i32 s80, s14, 64
	s_cmp_lt_u32 s8, 3
	s_cselect_b32 s80, s13, s80
	s_mul_i32 s81, s80, 0xc00
	s_add_i32 s85, s82, 0x8000
	s_mov_b32 m0, s85
	s_add_i32 s85, s82, 0x10000
	buffer_load_dwordx4 v154, s[72:75], s81 offen lds
	v_exp_f32_e32 v216, v128
	v_add_f32_e32 v128, 0, v222
	v_add_f32_e32 v128, v224, v128
	v_add_f32_e32 v128, v220, v128
	v_add_f32_e32 v128, v223, v128
	v_add_f32_e32 v128, v219, v128
	v_add_f32_e32 v128, v221, v128
	s_waitcnt lgkmcnt(6)
	v_mfma_f32_32x32x16_bf16 v[64:79], v[68:71], v[124:127], 0
	s_mov_b32 m0, s85
	s_add_i32 s85, s82, 0xa000
	buffer_load_dwordx4 v155, s[72:75], s81 offen lds
	v_add_f32_e32 v128, v217, v128
	v_add_f32_e32 v128, v218, v128
	v_add_f32_e32 v128, v212, v128
	v_add_f32_e32 v128, v214, v128
	v_add_f32_e32 v128, v211, v128
	v_add_f32_e32 v128, v213, v128
	v_exp_f32_e32 v138, v138
	s_waitcnt lgkmcnt(5)
	v_mfma_f32_32x32x16_bf16 v[80:95], v[200:203], v[120:123], v[80:95]
	s_mov_b32 m0, s85
	s_add_i32 s81, s81, 0x18000
	buffer_load_dwordx4 v154, s[72:75], s81 offen lds
	v_add_f32_e32 v128, v208, v128
	v_exp_f32_e32 v139, v139
	v_add_f32_e32 v128, v210, v128
	v_exp_f32_e32 v164, v136
	v_add_f32_e32 v128, v207, v128
	v_exp_f32_e32 v137, v137
	v_add_f32_e32 v128, v209, v128
	s_waitcnt lgkmcnt(4)
	v_mfma_f32_32x32x16_bf16 v[64:79], v[226:229], v[120:123], v[64:79]
	s_lshl_b32 s81, s83, 11
	s_add_i32 s85, s82, 0x4000
	s_mov_b32 m0, s85
	s_add_i32 s85, s82, 0x6000
	buffer_load_dwordx4 v158, s[76:79], s81 offen lds
	ds_read_b128 v[200:203], v184 offset:49152
	ds_read_b128 v[226:229], v184 offset:57344
	v_exp_f32_e32 v165, v132
	v_add_f32_e32 v128, v138, v128
	v_add_f32_e32 v128, v139, v128
	v_exp_f32_e32 v206, v130
	v_add_f32_e32 v128, v164, v128
	v_exp_f32_e32 v215, v131
	s_waitcnt lgkmcnt(5)
	v_mfma_f32_32x32x16_bf16 v[80:95], v[230:233], v[116:119], v[80:95]
	s_mov_b32 m0, s85
	s_add_i32 s81, s81, 0x10000
	buffer_load_dwordx4 v158, s[76:79], s81 offen lds
	s_mov_b32 s84, s80
	v_add_f32_e32 v128, v137, v128
	v_add_f32_e32 v128, v165, v128
	v_exp_f32_e32 v225, v129
	v_exp_f32_e32 v162, v162
	v_exp_f32_e32 v163, v163
	v_exp_f32_e32 v160, v160
	v_exp_f32_e32 v161, v161
	s_waitcnt lgkmcnt(4)
	v_mfma_f32_32x32x16_bf16 v[64:79], v[234:237], v[116:119], v[64:79]
	ds_read_b128 v[230:233], v185 offset:49152
	ds_read_b128 v[234:237], v185 offset:57344
	v_cvt_pk_bf16_f32 v129, v220, v223
	v_cvt_pk_bf16_f32 v130, v219, v221
	v_cvt_pk_bf16_f32 v131, v217, v218
	v_cvt_pk_bf16_f32 v132, v212, v214
	v_cvt_pk_bf16_f32 v136, v138, v139
	v_cvt_pk_bf16_f32 v137, v164, v137
	s_waitcnt lgkmcnt(5)
	v_mfma_f32_32x32x16_bf16 v[80:95], v[238:241], v[112:115], v[80:95]
	v_cvt_pk_bf16_f32 v139, v206, v215
	v_permlane32_swap_b32_e32 v129, v131
	s_nop 0
	v_permlane32_swap_b32_e32 v137, v139
	s_waitcnt lgkmcnt(4)
	v_mfma_f32_32x32x16_bf16 v[64:79], v[242:245], v[112:115], v[64:79]
	ds_read_b128 v[238:241], v186 offset:49152
	ds_read_b128 v[242:245], v186 offset:57344
	s_waitcnt lgkmcnt(5)
	v_mfma_f32_32x32x16_bf16 v[80:95], v[200:203], v[108:111], v[80:95]
	s_waitcnt lgkmcnt(4)
	v_mfma_f32_32x32x16_bf16 v[64:79], v[226:229], v[108:111], v[64:79]
	ds_read_b128 v[200:203], v187 offset:49152
	ds_read_b128 v[226:229], v187 offset:57344
	s_waitcnt lgkmcnt(5)
	v_mfma_f32_32x32x16_bf16 v[80:95], v[230:233], v[104:107], v[80:95]
	s_waitcnt lgkmcnt(4)
	v_mfma_f32_32x32x16_bf16 v[64:79], v[234:237], v[104:107], v[64:79]
	ds_read_b128 v[230:233], v199
	ds_read_b128 v[234:237], v199 offset:4096
	ds_read_b128 v[246:249], v190
	s_waitcnt lgkmcnt(6)
	v_mfma_f32_32x32x16_bf16 v[80:95], v[238:241], v[100:103], v[80:95]
	s_waitcnt lgkmcnt(5)
	v_mfma_f32_32x32x16_bf16 v[64:79], v[242:245], v[100:103], v[64:79]
	ds_read_b128 v[238:241], v204
	ds_read_b128 v[242:245], v204 offset:4096
	ds_read_b128 v[250:253], v190 offset:1024
	v_add_u32_e32 v204, s6, v173
	s_waitcnt lgkmcnt(7)
	v_mfma_f32_32x32x16_bf16 v[80:95], v[200:203], v[96:99], v[80:95]
	s_waitcnt lgkmcnt(6)
	v_mfma_f32_32x32x16_bf16 v[64:79], v[226:229], v[96:99], v[64:79]
	ds_read_b128 v[200:203], v205
	ds_read_b128 v[226:229], v205 offset:4096
	s_waitcnt lgkmcnt(5)
	v_mfma_f32_32x32x16_bf16 v[80:95], v[230:233], v[246:249], v[80:95]
	s_waitcnt lgkmcnt(5)
	v_mfma_f32_32x32x16_bf16 v[64:79], v[234:237], v[246:249], v[64:79]
	ds_read_b128 v[230:233], v204
	ds_read_b128 v[234:237], v204 offset:4096
	ds_read_b128 v[246:249], v190 offset:2048
	s_waitcnt lgkmcnt(5)
	v_mfma_f32_32x32x16_bf16 v[80:95], v[238:241], v[250:253], v[80:95]
	s_waitcnt lgkmcnt(5)
	v_mfma_f32_32x32x16_bf16 v[64:79], v[242:245], v[250:253], v[64:79]
	ds_read_b128 v[250:253], v190 offset:3072
	s_waitcnt lgkmcnt(1)
	v_mfma_f32_32x32x16_bf16 v[80:95], v[200:203], v[246:249], v[80:95]
	v_exp_f32_e32 v205, v133
	v_cvt_pk_bf16_f32 v133, v211, v213
	v_cvt_pk_bf16_f32 v138, v165, v205
	v_add_f32_e32 v128, v205, v128
	v_add_f32_e32 v128, v206, v128
	v_add_f32_e32 v128, v215, v128
	s_waitcnt lgkmcnt(1)
	v_mfma_f32_32x32x16_bf16 v[64:79], v[226:229], v[246:249], v[64:79]
	v_add_f32_e32 v128, v216, v128
	v_add_f32_e32 v128, v225, v128
	v_add_f32_e32 v128, v162, v128
	v_add_f32_e32 v128, v163, v128
	v_add_f32_e32 v128, v160, v128
	v_add_f32_e32 v128, v161, v128
	s_waitcnt lgkmcnt(0)
	v_mfma_f32_32x32x16_bf16 v[80:95], v[230:233], v[250:253], v[80:95]
	v_exp_f32_e32 v226, v134
	v_exp_f32_e32 v227, v135
	v_cvt_pk_bf16_f32 v134, v208, v210
	v_cvt_pk_bf16_f32 v135, v207, v209
	v_add_f32_e32 v128, v226, v128
	v_add_f32_e32 v203, v227, v128
	v_mov_b32_e32 v204, v203
	s_waitcnt lgkmcnt(0)
	v_mfma_f32_32x32x16_bf16 v[64:79], v[234:237], v[250:253], v[64:79]
	s_nop 0
	v_permlane32_swap_b32_e32 v203, v204
	v_cvt_pk_bf16_f32 v128, v222, v224
	v_cvt_pk_bf16_f32 v208, v216, v225
	v_cvt_pk_bf16_f32 v209, v162, v163
	v_cvt_pk_bf16_f32 v210, v160, v161
	v_cvt_pk_bf16_f32 v211, v226, v227
	v_permlane32_swap_b32_e32 v132, v134
	v_permlane32_swap_b32_e32 v128, v130
	v_permlane32_swap_b32_e32 v133, v135
	v_permlane32_swap_b32_e32 v136, v138
	v_permlane32_swap_b32_e32 v208, v210
	v_permlane32_swap_b32_e32 v209, v211
	ds_read_b64_tr_b16 v[160:161], v167 offset:0
	ds_read_b64_tr_b16 v[162:163], v167 offset:0x800
	ds_read_b64_tr_b16 v[232:233], v167 offset:0x1000
	ds_read_b64_tr_b16 v[234:235], v167 offset:0x1800
	ds_read_b64_tr_b16 v[236:237], v167 offset:0x2000
	ds_read_b64_tr_b16 v[238:239], v167 offset:0x2800
	ds_read_b64_tr_b16 v[240:241], v167 offset:0x3000
	ds_read_b64_tr_b16 v[242:243], v167 offset:0x3800
	v_max_f32_e32 v164, v81, v81
	v_max_f32_e32 v165, v80, v80
	v_max_f32_e32 v164, v165, v164
	v_max3_f32 v164, v164, v82, v83
	v_max3_f32 v164, v164, v84, v85
	v_max3_f32 v164, v164, v86, v87
	v_max3_f32 v164, v164, v88, v89
	v_max3_f32 v164, v164, v90, v91
	v_max3_f32 v164, v164, v92, v93
	v_max3_f32 v164, v164, v94, v95
	s_waitcnt lgkmcnt(0)
	v_mfma_f32_32x32x16_bf16 v[0:15], v[128:131], v[160:163], v[0:15]
	v_max3_f32 v160, v164, v64, v65
	v_max3_f32 v160, v160, v66, v67
	v_max3_f32 v160, v160, v68, v69
	v_mfma_f32_32x32x16_bf16 v[0:15], v[132:135], v[232:235], v[0:15]
	ds_read_b64_tr_b16 v[232:233], v167 offset:0x200
	ds_read_b64_tr_b16 v[234:235], v167 offset:0xa00
	v_max3_f32 v160, v160, v70, v71
	v_max3_f32 v160, v160, v72, v73
	v_max3_f32 v160, v160, v74, v75
	v_mfma_f32_32x32x16_bf16 v[0:15], v[136:139], v[236:239], v[0:15]
	ds_read_b64_tr_b16 v[236:237], v167 offset:0x1200
	ds_read_b64_tr_b16 v[238:239], v167 offset:0x1a00
	ds_read_b64_tr_b16 v[244:245], v167 offset:0x2200
	ds_read_b64_tr_b16 v[246:247], v167 offset:0x2a00
	ds_read_b64_tr_b16 v[248:249], v167 offset:0x3200
	ds_read_b64_tr_b16 v[250:251], v167 offset:0x3a00
	v_max3_f32 v160, v160, v76, v77
	v_max3_f32 v160, v160, v78, v79
	v_mov_b32_e32 v161, v160
	v_mfma_f32_32x32x16_bf16 v[0:15], v[208:211], v[240:243], v[0:15]
	v_max_f32_e32 v162, v198, v198
	v_permlane32_swap_b32_e32 v160, v161
	v_max_f32_e32 v161, v161, v161
	v_max_f32_e32 v160, v160, v160
	v_max_f32_e32 v160, v160, v161
	s_waitcnt lgkmcnt(0)
	v_mfma_f32_32x32x16_bf16 v[32:47], v[128:131], v[232:235], v[32:47]
	ds_read_b64_tr_b16 v[232:233], v167 offset:0x400
	ds_read_b64_tr_b16 v[234:235], v167 offset:0xc00
	v_sub_f32_e32 v161, v160, v198
	v_max_f32_e32 v160, v162, v160
	v_sub_f32_e32 v162, v198, v160
	v_mul_f32_e32 v162, 0x3dd53b94, v162
	v_exp_f32_e32 v162, v162
	v_mfma_f32_32x32x16_bf16 v[32:47], v[132:135], v[236:239], v[32:47]
	ds_read_b64_tr_b16 v[236:237], v167 offset:0x1400
	ds_read_b64_tr_b16 v[238:239], v167 offset:0x1c00
	ds_read_b64_tr_b16 v[240:241], v167 offset:0x2400
	ds_read_b64_tr_b16 v[242:243], v167 offset:0x2c00
	v_cmp_ge_f32_e32 vcc, s46, v161
	s_cmp_eq_u64 vcc, exec
	s_cselect_b64 s[6:7], -1, 0
	v_cndmask_b32_e64 v206, v162, 1.0, s[6:7]
	v_cndmask_b32_e64 v160, v160, v198, s[6:7]
	v_mul_f32_e32 v205, 0xbdd53b94, v160
	v_cmp_gt_f32_e32 vcc, 1.0, v206
	v_mfma_f32_32x32x16_bf16 v[32:47], v[136:139], v[244:247], v[32:47]
	ds_read_b64_tr_b16 v[244:245], v167 offset:0x3400
	ds_read_b64_tr_b16 v[246:247], v167 offset:0x3c00
	v_pk_fma_f32 v[86:87], v[86:87], s[26:27], v[204:205] op_sel:[0,0,1] op_sel_hi:[1,0,1]
	v_pk_fma_f32 v[80:81], v[80:81], s[26:27], v[204:205] op_sel:[0,0,1] op_sel_hi:[1,0,1]
	v_pk_fma_f32 v[82:83], v[82:83], s[26:27], v[204:205] op_sel:[0,0,1] op_sel_hi:[1,0,1]
	v_mfma_f32_32x32x16_bf16 v[32:47], v[208:211], v[248:251], v[32:47]
	v_pk_fma_f32 v[84:85], v[84:85], s[26:27], v[204:205] op_sel:[0,0,1] op_sel_hi:[1,0,1]
	v_pk_fma_f32 v[88:89], v[88:89], s[26:27], v[204:205] op_sel:[0,0,1] op_sel_hi:[1,0,1]
	s_waitcnt lgkmcnt(0)
	v_mfma_f32_32x32x16_bf16 v[16:31], v[128:131], v[232:235], v[16:31]
	ds_read_b64_tr_b16 v[232:233], v167 offset:0x600
	ds_read_b64_tr_b16 v[234:235], v167 offset:0xe00
	v_pk_fma_f32 v[90:91], v[90:91], s[26:27], v[204:205] op_sel:[0,0,1] op_sel_hi:[1,0,1]
	v_pk_fma_f32 v[92:93], v[92:93], s[26:27], v[204:205] op_sel:[0,0,1] op_sel_hi:[1,0,1]
	v_pk_fma_f32 v[94:95], v[94:95], s[26:27], v[204:205] op_sel:[0,0,1] op_sel_hi:[1,0,1]
	v_mfma_f32_32x32x16_bf16 v[16:31], v[132:135], v[236:239], v[16:31]
	ds_read_b64_tr_b16 v[236:237], v167 offset:0x1600
	ds_read_b64_tr_b16 v[238:239], v167 offset:0x1e00
	v_fmamk_f32 v215, v64, 0x3dd53b94, v205
	v_fmamk_f32 v216, v65, 0x3dd53b94, v205
	v_fmamk_f32 v217, v66, 0x3dd53b94, v205
	v_fmamk_f32 v218, v67, 0x3dd53b94, v205
	v_mfma_f32_32x32x16_bf16 v[16:31], v[136:139], v[240:243], v[16:31]
	ds_read_b64_tr_b16 v[240:241], v167 offset:0x2600
	ds_read_b64_tr_b16 v[242:243], v167 offset:0x2e00
	ds_read_b64_tr_b16 v[248:249], v167 offset:0x3600
	ds_read_b64_tr_b16 v[250:251], v167 offset:0x3e00
	v_fmamk_f32 v219, v68, 0x3dd53b94, v205
	v_fmamk_f32 v212, v73, 0x3dd53b94, v205
	v_fmamk_f32 v213, v74, 0x3dd53b94, v205
	v_fmamk_f32 v214, v75, 0x3dd53b94, v205
	v_mfma_f32_32x32x16_bf16 v[16:31], v[208:211], v[244:247], v[16:31]
	v_fmamk_f32 v207, v76, 0x3dd53b94, v205
	v_fmamk_f32 v220, v77, 0x3dd53b94, v205
	v_fmamk_f32 v221, v78, 0x3dd53b94, v205
	s_waitcnt lgkmcnt(0)
	v_mfma_f32_32x32x16_bf16 v[48:63], v[128:131], v[232:235], v[48:63]
	v_exp_f32_e32 v128, v80
	v_exp_f32_e32 v129, v82
	v_exp_f32_e32 v130, v84
	v_exp_f32_e32 v131, v86
	v_mfma_f32_32x32x16_bf16 v[48:63], v[132:135], v[236:239], v[48:63]
	v_exp_f32_e32 v132, v88
	v_exp_f32_e32 v133, v90
	v_exp_f32_e32 v134, v92
	v_exp_f32_e32 v135, v94
	v_mfma_f32_32x32x16_bf16 v[48:63], v[136:139], v[240:243], v[48:63]
	v_exp_f32_e32 v139, v89
	v_exp_f32_e32 v138, v91
	v_exp_f32_e32 v137, v93
	v_exp_f32_e32 v136, v95
	v_mfma_f32_32x32x16_bf16 v[48:63], v[208:211], v[248:251], v[48:63]
	v_exp_f32_e32 v161, v87
	v_exp_f32_e32 v198, v81
	v_exp_f32_e32 v163, v83
	v_exp_f32_e32 v162, v85
	v_fmamk_f32 v208, v69, 0x3dd53b94, v205
	v_fmamk_f32 v209, v70, 0x3dd53b94, v205
	v_fmamk_f32 v210, v71, 0x3dd53b94, v205
	v_fmamk_f32 v211, v72, 0x3dd53b94, v205
	v_fmac_f32_e32 v205, 0x3dd53b94, v79
	s_cbranch_vccz .LBB0_2016
	s_and_saveexec_b64 s[10:11], s[4:5]
	ds_write_b32 v189, v206 offset:128
	s_or_b64 exec, exec, s[10:11]
	s_waitcnt lgkmcnt(0)
	v_add_u32_e32 v248, s12, v169
	ds_read_b128 v[232:235], v248 offset:224
	ds_read_b128 v[236:239], v248 offset:192
	ds_read_b128 v[240:243], v248 offset:160
	ds_read_b128 v[244:247], v248 offset:128
	s_waitcnt lgkmcnt(3)
	v_pk_mul_f32 v[12:13], v[12:13], v[232:233]
	s_waitcnt lgkmcnt(2)
	v_pk_mul_f32 v[8:9], v[8:9], v[236:237]
	s_waitcnt lgkmcnt(1)
	v_pk_mul_f32 v[4:5], v[4:5], v[240:241]
	v_pk_mul_f32 v[14:15], v[14:15], v[234:235]
	v_pk_mul_f32 v[10:11], v[10:11], v[238:239]
	v_pk_mul_f32 v[6:7], v[6:7], v[242:243]
	s_waitcnt lgkmcnt(0)
	v_pk_mul_f32 v[2:3], v[2:3], v[246:247]
	v_pk_mul_f32 v[0:1], v[0:1], v[244:245]
	v_pk_mul_f32 v[44:45], v[44:45], v[232:233]
	v_pk_mul_f32 v[40:41], v[40:41], v[236:237]
	v_pk_mul_f32 v[36:37], v[36:37], v[240:241]
	v_pk_mul_f32 v[46:47], v[46:47], v[234:235]
	v_pk_mul_f32 v[42:43], v[42:43], v[238:239]
	v_pk_mul_f32 v[38:39], v[38:39], v[242:243]
	v_pk_mul_f32 v[34:35], v[34:35], v[246:247]
	v_pk_mul_f32 v[32:33], v[32:33], v[244:245]
	v_pk_mul_f32 v[28:29], v[28:29], v[232:233]
	v_pk_mul_f32 v[24:25], v[24:25], v[236:237]
	v_pk_mul_f32 v[20:21], v[20:21], v[240:241]
	v_pk_mul_f32 v[30:31], v[30:31], v[234:235]
	v_pk_mul_f32 v[26:27], v[26:27], v[238:239]
	v_pk_mul_f32 v[22:23], v[22:23], v[242:243]
	v_pk_mul_f32 v[18:19], v[18:19], v[246:247]
	v_pk_mul_f32 v[16:17], v[16:17], v[244:245]
	v_pk_mul_f32 v[60:61], v[60:61], v[232:233]
	v_pk_mul_f32 v[56:57], v[56:57], v[236:237]
	v_pk_mul_f32 v[52:53], v[52:53], v[240:241]
	v_pk_mul_f32 v[62:63], v[62:63], v[234:235]
	v_pk_mul_f32 v[58:59], v[58:59], v[238:239]
	v_pk_mul_f32 v[54:55], v[54:55], v[242:243]
	v_pk_mul_f32 v[50:51], v[50:51], v[246:247]
	v_pk_mul_f32 v[48:49], v[48:49], v[244:245]
.LBB0_2016:
	s_waitcnt vmcnt(0) lgkmcnt(0)
	s_barrier
	ds_read_b128 v[64:67], v180 offset:32768
	ds_read_b128 v[68:71], v180 offset:40960
	ds_read_b128 v[222:225], v181 offset:32768
	ds_read_b128 v[226:229], v181 offset:40960
	ds_read_b128 v[230:233], v182 offset:32768
	ds_read_b128 v[234:237], v182 offset:40960
	ds_read_b128 v[238:241], v183 offset:32768
	ds_read_b128 v[242:245], v183 offset:40960
	v_exp_f32_e32 v164, v215
	v_add_f32_e32 v215, 0, v128
	s_waitcnt lgkmcnt(7)
	v_mfma_f32_32x32x16_bf16 v[80:95], v[64:67], v[124:127], 0
	s_add_i32 s80, s13, 64
	s_cmp_lt_u32 s8, 2
	s_cselect_b32 s80, s80, s14
	s_mul_i32 s81, s80, 0xc00
	s_add_i32 s85, s82, 0xc000
	s_mov_b32 m0, s85
	s_add_i32 s85, s82, 0x12000
	buffer_load_dwordx4 v154, s[72:75], s81 offen lds
	v_add_f32_e32 v215, v198, v215
	v_add_f32_e32 v215, v129, v215
	v_add_f32_e32 v215, v163, v215
	v_add_f32_e32 v215, v130, v215
	v_add_f32_e32 v215, v162, v215
	v_add_f32_e32 v215, v131, v215
	v_add_f32_e32 v215, v161, v215
	s_waitcnt lgkmcnt(6)
	v_mfma_f32_32x32x16_bf16 v[64:79], v[68:71], v[124:127], 0
	s_mov_b32 m0, s85
	s_add_i32 s85, s82, 0xe000
	buffer_load_dwordx4 v155, s[72:75], s81 offen lds
	v_add_f32_e32 v215, v132, v215
	v_add_f32_e32 v215, v139, v215
	v_add_f32_e32 v215, v133, v215
	v_add_f32_e32 v215, v138, v215
	v_add_f32_e32 v215, v134, v215
	v_exp_f32_e32 v165, v216
	v_add_f32_e32 v215, v137, v215
	s_waitcnt lgkmcnt(5)
	v_mfma_f32_32x32x16_bf16 v[80:95], v[222:225], v[120:123], v[80:95]
	s_mov_b32 m0, s85
	s_add_i32 s81, s81, 0x18000
	buffer_load_dwordx4 v154, s[72:75], s81 offen lds
	v_exp_f32_e32 v217, v217
	v_add_f32_e32 v215, v135, v215
	v_exp_f32_e32 v218, v218
	v_add_f32_e32 v215, v136, v215
	v_exp_f32_e32 v219, v219
	v_add_f32_e32 v215, v164, v215
	v_exp_f32_e32 v208, v208
	s_waitcnt lgkmcnt(4)
	v_mfma_f32_32x32x16_bf16 v[64:79], v[226:229], v[120:123], v[64:79]
	s_lshl_b32 s81, s84, 11
	s_add_i32 s85, s82, 0x0
	s_mov_b32 m0, s85
	s_add_i32 s85, s82, 0x2000
	buffer_load_dwordx4 v158, s[76:79], s81 offen lds
	ds_read_b128 v[222:225], v184 offset:32768
	ds_read_b128 v[226:229], v184 offset:40960
	v_add_f32_e32 v215, v165, v215
	v_exp_f32_e32 v209, v209
	v_add_f32_e32 v215, v217, v215
	v_exp_f32_e32 v210, v210
	v_add_f32_e32 v215, v218, v215
	v_exp_f32_e32 v211, v211
	s_waitcnt lgkmcnt(5)
	v_mfma_f32_32x32x16_bf16 v[80:95], v[230:233], v[116:119], v[80:95]
	s_mov_b32 m0, s85
	s_add_i32 s81, s81, 0x10000
	buffer_load_dwordx4 v158, s[76:79], s81 offen lds
	s_mov_b32 s83, s80
	v_add_f32_e32 v215, v219, v215
	v_exp_f32_e32 v212, v212
	v_add_f32_e32 v215, v208, v215
	v_exp_f32_e32 v213, v213
	v_add_f32_e32 v215, v209, v215
	v_exp_f32_e32 v214, v214
	v_add_f32_e32 v215, v210, v215
	s_waitcnt lgkmcnt(4)
	v_mfma_f32_32x32x16_bf16 v[64:79], v[234:237], v[116:119], v[64:79]
	ds_read_b128 v[230:233], v185 offset:32768
	ds_read_b128 v[234:237], v185 offset:40960
	v_exp_f32_e32 v207, v207
	v_add_f32_e32 v215, v211, v215
	v_exp_f32_e32 v220, v220
	v_add_f32_e32 v215, v212, v215
	v_exp_f32_e32 v221, v221
	v_add_f32_e32 v215, v213, v215
	s_waitcnt lgkmcnt(5)
	v_mfma_f32_32x32x16_bf16 v[80:95], v[238:241], v[112:115], v[80:95]
	v_exp_f32_e32 v205, v205
	v_add_f32_e32 v215, v214, v215
	v_add_f32_e32 v215, v207, v215
	v_add_f32_e32 v215, v220, v215
	v_add_f32_e32 v215, v221, v215
	v_add_f32_e32 v215, v205, v215
	v_mov_b32_e32 v216, v215
	s_waitcnt lgkmcnt(4)
	v_mfma_f32_32x32x16_bf16 v[64:79], v[242:245], v[112:115], v[64:79]
	ds_read_b128 v[238:241], v186 offset:32768
	ds_read_b128 v[242:245], v186 offset:40960
	v_permlane32_swap_b32_e32 v215, v216
	v_cvt_pk_bf16_f32 v128, v128, v198
	v_cvt_pk_bf16_f32 v129, v129, v163
	v_cvt_pk_bf16_f32 v130, v130, v162
	v_cvt_pk_bf16_f32 v131, v131, v161
	s_waitcnt lgkmcnt(5)
	v_mfma_f32_32x32x16_bf16 v[80:95], v[222:225], v[108:111], v[80:95]
	v_cvt_pk_bf16_f32 v132, v132, v139
	v_cvt_pk_bf16_f32 v133, v133, v138
	v_cvt_pk_bf16_f32 v134, v134, v137
	v_cvt_pk_bf16_f32 v135, v135, v136
	v_cvt_pk_bf16_f32 v136, v164, v165
	v_cvt_pk_bf16_f32 v137, v217, v218
	v_cvt_pk_bf16_f32 v138, v219, v208
	s_waitcnt lgkmcnt(4)
	v_mfma_f32_32x32x16_bf16 v[64:79], v[226:229], v[108:111], v[64:79]
	ds_read_b128 v[222:225], v187 offset:32768
	ds_read_b128 v[226:229], v187 offset:40960
	v_cvt_pk_bf16_f32 v139, v209, v210
	v_cvt_pk_bf16_f32 v208, v211, v212
	v_cvt_pk_bf16_f32 v209, v213, v214
	v_cvt_pk_bf16_f32 v210, v207, v220
	v_cvt_pk_bf16_f32 v211, v221, v205
	v_permlane32_swap_b32_e32 v128, v130
	s_waitcnt lgkmcnt(5)
	v_mfma_f32_32x32x16_bf16 v[80:95], v[230:233], v[104:107], v[80:95]
	v_permlane32_swap_b32_e32 v129, v131
	v_permlane32_swap_b32_e32 v132, v134
	v_permlane32_swap_b32_e32 v133, v135
	v_permlane32_swap_b32_e32 v136, v138
	s_waitcnt lgkmcnt(4)
	v_mfma_f32_32x32x16_bf16 v[64:79], v[234:237], v[104:107], v[64:79]
	ds_read_b128 v[230:233], v191
	ds_read_b128 v[234:237], v191 offset:4096
	ds_read_b128 v[246:249], v190
	v_permlane32_swap_b32_e32 v137, v139
	v_permlane32_swap_b32_e32 v208, v210
	v_permlane32_swap_b32_e32 v209, v211
	s_waitcnt lgkmcnt(6)
	v_mfma_f32_32x32x16_bf16 v[80:95], v[238:241], v[100:103], v[80:95]
	s_waitcnt lgkmcnt(5)
	v_mfma_f32_32x32x16_bf16 v[64:79], v[242:245], v[100:103], v[64:79]
	ds_read_b128 v[238:241], v192
	ds_read_b128 v[242:245], v192 offset:4096
	ds_read_b128 v[250:253], v190 offset:1024
	s_waitcnt lgkmcnt(7)
	v_mfma_f32_32x32x16_bf16 v[80:95], v[222:225], v[96:99], v[80:95]
	s_waitcnt lgkmcnt(6)
	v_mfma_f32_32x32x16_bf16 v[64:79], v[226:229], v[96:99], v[64:79]
	ds_read_b128 v[222:225], v193
	ds_read_b128 v[226:229], v193 offset:4096
	s_waitcnt lgkmcnt(5)
	v_mfma_f32_32x32x16_bf16 v[80:95], v[230:233], v[246:249], v[80:95]
	s_waitcnt lgkmcnt(5)
	v_mfma_f32_32x32x16_bf16 v[64:79], v[234:237], v[246:249], v[64:79]
	ds_read_b128 v[230:233], v194
	ds_read_b128 v[234:237], v194 offset:4096
	ds_read_b128 v[246:249], v190 offset:2048
	s_waitcnt lgkmcnt(5)
	v_mfma_f32_32x32x16_bf16 v[80:95], v[238:241], v[250:253], v[80:95]
	s_waitcnt lgkmcnt(5)
	v_mfma_f32_32x32x16_bf16 v[64:79], v[242:245], v[250:253], v[64:79]
	ds_read_b128 v[250:253], v190 offset:3072
	s_waitcnt lgkmcnt(1)
	v_mfma_f32_32x32x16_bf16 v[80:95], v[222:225], v[246:249], v[80:95]
	s_waitcnt lgkmcnt(1)
	v_mfma_f32_32x32x16_bf16 v[64:79], v[226:229], v[246:249], v[64:79]
	s_waitcnt lgkmcnt(0)
	v_mfma_f32_32x32x16_bf16 v[80:95], v[230:233], v[250:253], v[80:95]
	s_waitcnt lgkmcnt(0)
	v_mfma_f32_32x32x16_bf16 v[64:79], v[234:237], v[250:253], v[64:79]
	ds_read_b64_tr_b16 v[238:239], v174 offset:0
	ds_read_b64_tr_b16 v[240:241], v174 offset:0x800
	ds_read_b64_tr_b16 v[242:243], v174 offset:0x1000
	ds_read_b64_tr_b16 v[244:245], v174 offset:0x1800
	ds_read_b64_tr_b16 v[246:247], v174 offset:0x2000
	ds_read_b64_tr_b16 v[248:249], v174 offset:0x2800
	ds_read_b64_tr_b16 v[250:251], v174 offset:0x3000
	ds_read_b64_tr_b16 v[252:253], v174 offset:0x3800
	s_nop 3
	v_max_f32_e32 v161, v81, v81
	v_max_f32_e32 v162, v80, v80
	v_max_f32_e32 v161, v162, v161
	v_max3_f32 v161, v161, v82, v83
	v_max3_f32 v161, v161, v84, v85
	v_max3_f32 v161, v161, v86, v87
	v_max3_f32 v161, v161, v88, v89
	v_max3_f32 v161, v161, v90, v91
	v_max3_f32 v161, v161, v92, v93
	v_max3_f32 v161, v161, v94, v95
	s_waitcnt lgkmcnt(0)
	v_mfma_f32_32x32x16_bf16 v[0:15], v[128:131], v[238:241], v[0:15]
	ds_read_b64_tr_b16 v[238:239], v174 offset:0x200
	ds_read_b64_tr_b16 v[240:241], v174 offset:0xa00
	v_max3_f32 v161, v161, v64, v65
	v_max3_f32 v161, v161, v66, v67
	v_max3_f32 v161, v161, v68, v69
	v_mfma_f32_32x32x16_bf16 v[0:15], v[132:135], v[242:245], v[0:15]
	ds_read_b64_tr_b16 v[242:243], v174 offset:0x1200
	ds_read_b64_tr_b16 v[244:245], v174 offset:0x1a00
	v_max3_f32 v161, v161, v70, v71
	v_max3_f32 v161, v161, v72, v73
	v_max3_f32 v161, v161, v74, v75
	v_mfma_f32_32x32x16_bf16 v[0:15], v[136:139], v[246:249], v[0:15]
	ds_read_b64_tr_b16 v[246:247], v174 offset:0x2200
	ds_read_b64_tr_b16 v[248:249], v174 offset:0x2a00
	ds_read_b64_tr_b16 v[162:163], v174 offset:0x3200
	ds_read_b64_tr_b16 v[164:165], v174 offset:0x3a00
	v_max3_f32 v161, v161, v76, v77
	v_max3_f32 v161, v161, v78, v79
	v_mov_b32_e32 v198, v161
	v_mfma_f32_32x32x16_bf16 v[0:15], v[208:211], v[250:253], v[0:15]
	v_max_f32_e32 v205, v160, v160
	v_permlane32_swap_b32_e32 v161, v198
	v_max_f32_e32 v198, v198, v198
	v_max_f32_e32 v161, v161, v161
	v_max_f32_e32 v161, v161, v198
	s_waitcnt lgkmcnt(0)
	v_mfma_f32_32x32x16_bf16 v[32:47], v[128:131], v[238:241], v[32:47]
	ds_read_b64_tr_b16 v[238:239], v174 offset:0x400
	ds_read_b64_tr_b16 v[240:241], v174 offset:0xc00
	v_sub_f32_e32 v198, v161, v160
	v_max_f32_e32 v161, v205, v161
	v_sub_f32_e32 v205, v160, v161
	v_mul_f32_e32 v205, 0x3dd53b94, v205
	v_exp_f32_e32 v205, v205
	v_mfma_f32_32x32x16_bf16 v[32:47], v[132:135], v[242:245], v[32:47]
	ds_read_b64_tr_b16 v[242:243], v174 offset:0x1400
	ds_read_b64_tr_b16 v[244:245], v174 offset:0x1c00
	v_cmp_ge_f32_e32 vcc, s46, v198
	s_cmp_eq_u64 vcc, exec
	s_cselect_b64 s[6:7], -1, 0
	v_cndmask_b32_e64 v205, v205, 1.0, s[6:7]
	v_cndmask_b32_e64 v198, v161, v160, s[6:7]
	v_mul_f32_e32 v236, 0xbdd53b94, v198
	v_mov_b32_e32 v237, v236
	v_cmp_gt_f32_e32 vcc, 1.0, v205
	v_mfma_f32_32x32x16_bf16 v[32:47], v[136:139], v[246:249], v[32:47]
	ds_read_b64_tr_b16 v[246:247], v174 offset:0x2400
	ds_read_b64_tr_b16 v[248:249], v174 offset:0x2c00
	ds_read_b64_tr_b16 v[250:251], v174 offset:0x3400
	ds_read_b64_tr_b16 v[252:253], v174 offset:0x3c00
	v_pk_fma_f32 v[80:81], v[80:81], s[26:27], v[236:237] op_sel_hi:[1,0,0]
	v_pk_fma_f32 v[82:83], v[82:83], s[26:27], v[236:237] op_sel_hi:[1,0,0]
	v_mfma_f32_32x32x16_bf16 v[32:47], v[208:211], v[162:165], v[32:47]
	v_pk_fma_f32 v[84:85], v[84:85], s[26:27], v[236:237] op_sel_hi:[1,0,0]
	v_pk_fma_f32 v[86:87], v[86:87], s[26:27], v[236:237] op_sel_hi:[1,0,0]
	s_waitcnt lgkmcnt(0)
	v_mfma_f32_32x32x16_bf16 v[16:31], v[128:131], v[238:241], v[16:31]
	ds_read_b64_tr_b16 v[162:163], v174 offset:0x600
	ds_read_b64_tr_b16 v[164:165], v174 offset:0xe00
	ds_read_b64_tr_b16 v[238:239], v174 offset:0x1600
	ds_read_b64_tr_b16 v[240:241], v174 offset:0x1e00
	v_pk_fma_f32 v[88:89], v[88:89], s[26:27], v[236:237] op_sel_hi:[1,0,0]
	v_pk_fma_f32 v[90:91], v[90:91], s[26:27], v[236:237] op_sel_hi:[1,0,0]
	v_mfma_f32_32x32x16_bf16 v[16:31], v[132:135], v[242:245], v[16:31]
	ds_read_b64_tr_b16 v[242:243], v174 offset:0x2600
	ds_read_b64_tr_b16 v[244:245], v174 offset:0x2e00
	v_pk_fma_f32 v[92:93], v[92:93], s[26:27], v[236:237] op_sel_hi:[1,0,0]
	v_pk_fma_f32 v[94:95], v[94:95], s[26:27], v[236:237] op_sel_hi:[1,0,0]
	v_mfma_f32_32x32x16_bf16 v[16:31], v[136:139], v[246:249], v[16:31]
	ds_read_b64_tr_b16 v[246:247], v174 offset:0x3600
	ds_read_b64_tr_b16 v[248:249], v174 offset:0x3e00
	v_exp_f32_e32 v222, v80
	v_exp_f32_e32 v224, v81
	v_exp_f32_e32 v220, v82
	v_mfma_f32_32x32x16_bf16 v[16:31], v[208:211], v[250:253], v[16:31]
	v_exp_f32_e32 v223, v83
	v_exp_f32_e32 v219, v84
	v_exp_f32_e32 v221, v85
	s_waitcnt lgkmcnt(0)
	v_mfma_f32_32x32x16_bf16 v[48:63], v[128:131], v[162:165], v[48:63]
	v_exp_f32_e32 v217, v86
	v_exp_f32_e32 v218, v87
	v_exp_f32_e32 v212, v88
	v_pk_fma_f32 v[130:131], v[70:71], s[26:27], v[236:237] op_sel_hi:[1,0,0]
	v_pk_fma_f32 v[128:129], v[72:73], s[26:27], v[236:237] op_sel_hi:[1,0,0]
	v_mfma_f32_32x32x16_bf16 v[48:63], v[132:135], v[238:241], v[48:63]
	v_exp_f32_e32 v214, v89
	v_exp_f32_e32 v213, v91
	v_exp_f32_e32 v207, v94
	v_pk_fma_f32 v[132:133], v[68:69], s[26:27], v[236:237] op_sel_hi:[1,0,0]
	v_pk_fma_f32 v[134:135], v[78:79], s[26:27], v[236:237] op_sel_hi:[1,0,0]
	v_mfma_f32_32x32x16_bf16 v[48:63], v[136:139], v[242:245], v[48:63]
	v_pk_fma_f32 v[138:139], v[64:65], s[26:27], v[236:237] op_sel_hi:[1,0,0]
	v_pk_fma_f32 v[136:137], v[66:67], s[26:27], v[236:237] op_sel_hi:[1,0,0]
	v_pk_fma_f32 v[162:163], v[74:75], s[26:27], v[236:237] op_sel_hi:[1,0,0]
	v_pk_fma_f32 v[160:161], v[76:77], s[26:27], v[236:237] op_sel_hi:[1,0,0]
	v_mfma_f32_32x32x16_bf16 v[48:63], v[208:211], v[246:249], v[48:63]
	v_exp_f32_e32 v211, v90
	v_exp_f32_e32 v208, v92
	v_exp_f32_e32 v210, v93
	v_exp_f32_e32 v209, v95
	v_add_f32_e32 v64, v203, v204
	v_fmac_f32_e32 v64, v197, v140
	v_add_f32_e32 v140, v215, v216
	s_addk_i32 s13, 0x80
	s_addk_i32 s14, 0x80
	v_fmac_f32_e32 v140, v64, v206
	s_cbranch_vccz .LBB0_2020
	s_and_saveexec_b64 s[10:11], s[4:5]
	ds_write_b32 v189, v205 offset:128
	s_or_b64 exec, exec, s[10:11]
	s_waitcnt lgkmcnt(0)
	v_add_u32_e32 v164, s12, v169
	ds_read_b128 v[238:241], v164 offset:224
	ds_read_b128 v[242:245], v164 offset:192
	ds_read_b128 v[246:249], v164 offset:160
	ds_read_b128 v[250:253], v164 offset:128
	s_waitcnt lgkmcnt(3)
	v_pk_mul_f32 v[12:13], v[12:13], v[238:239]
	s_waitcnt lgkmcnt(2)
	v_pk_mul_f32 v[8:9], v[8:9], v[242:243]
	s_waitcnt lgkmcnt(1)
	v_pk_mul_f32 v[4:5], v[4:5], v[246:247]
	v_pk_mul_f32 v[14:15], v[14:15], v[240:241]
	v_pk_mul_f32 v[10:11], v[10:11], v[244:245]
	v_pk_mul_f32 v[6:7], v[6:7], v[248:249]
	s_waitcnt lgkmcnt(0)
	v_pk_mul_f32 v[2:3], v[2:3], v[252:253]
	v_pk_mul_f32 v[0:1], v[0:1], v[250:251]
	v_pk_mul_f32 v[44:45], v[44:45], v[238:239]
	v_pk_mul_f32 v[40:41], v[40:41], v[242:243]
	v_pk_mul_f32 v[36:37], v[36:37], v[246:247]
	v_pk_mul_f32 v[46:47], v[46:47], v[240:241]
	v_pk_mul_f32 v[42:43], v[42:43], v[244:245]
	v_pk_mul_f32 v[38:39], v[38:39], v[248:249]
	v_pk_mul_f32 v[34:35], v[34:35], v[252:253]
	v_pk_mul_f32 v[32:33], v[32:33], v[250:251]
	v_pk_mul_f32 v[28:29], v[28:29], v[238:239]
	v_pk_mul_f32 v[24:25], v[24:25], v[242:243]
	v_pk_mul_f32 v[20:21], v[20:21], v[246:247]
	v_pk_mul_f32 v[30:31], v[30:31], v[240:241]
	v_pk_mul_f32 v[26:27], v[26:27], v[244:245]
	v_pk_mul_f32 v[22:23], v[22:23], v[248:249]
	v_pk_mul_f32 v[18:19], v[18:19], v[252:253]
	v_pk_mul_f32 v[16:17], v[16:17], v[250:251]
	v_pk_mul_f32 v[60:61], v[60:61], v[238:239]
	v_pk_mul_f32 v[56:57], v[56:57], v[242:243]
	v_pk_mul_f32 v[52:53], v[52:53], v[246:247]
	v_pk_mul_f32 v[62:63], v[62:63], v[240:241]
	v_pk_mul_f32 v[58:59], v[58:59], v[244:245]
	v_pk_mul_f32 v[54:55], v[54:55], v[248:249]
	v_pk_mul_f32 v[50:51], v[50:51], v[252:253]
	v_pk_mul_f32 v[48:49], v[48:49], v[250:251]
